# speedup vs baseline: 1.0842x; 1.0257x over previous
_Z5k_aggPKDF16_PKhPKiS4_PKDv8_DF16_PKfPDF16_Pf:
	s_load_dwordx8 s[4:11], s[0:1], 0x8
	s_load_dwordx4 s[12:15], s[0:1], 0x28
	s_load_dwordx2 s[16:17], s[0:1], 0x38
	v_lshlrev_b32_e32 v2, 4, v0
	s_lshl_b32 s0, s2, 2
	s_lshl_b32 s1, s2, 3
	s_andn2_b32 s0, s0, 63
	s_and_b32 s1, s1, 56
	s_or_b32 s0, s0, s1
	s_lshr_b32 s1, s2, 1
	s_and_b32 s1, s1, 4
	s_or_b32 s0, s0, s1
	v_lshlrev_b32_e32 v1, 2, v0
	v_lshrrev_b32_e32 v52, 6, v0
	v_or_b32_e32 v3, s0, v52
	v_mov_b32_e32 v98, v2
	s_waitcnt lgkmcnt(0)
	global_load_dwordx4 v[64:67], v2, s[10:11]
	v_add_u32_e32 v96, 0x1000, v2
	global_load_dwordx4 v[68:71], v96, s[10:11]
	v_add_u32_e32 v96, 0x2000, v2
	global_load_dwordx4 v[72:75], v96, s[10:11]
	v_add_u32_e32 v96, 0x3000, v2
	global_load_dwordx4 v[76:79], v96, s[10:11]
	v_add_u32_e32 v96, 0x4000, v2
	global_load_dwordx4 v[80:83], v96, s[10:11]
	v_add_u32_e32 v96, 0x5000, v2
	global_load_dwordx4 v[84:87], v96, s[10:11]
	v_add_u32_e32 v96, 0x6000, v2
	global_load_dwordx4 v[88:91], v96, s[10:11]
	v_add_u32_e32 v96, 0x7000, v2
	global_load_dwordx4 v[92:95], v96, s[10:11]
	v_mov_b32_e32 v97, 0
	ds_write2st64_b32 v1, v97, v97 offset0:128 offset1:132
	ds_write2st64_b32 v1, v97, v97 offset0:136 offset1:140
	s_movk_i32 s0, 0x186a
	v_cmp_gt_i32_e32 vcc, s0, v3
	s_and_saveexec_b64 s[0:1], vcc
	s_cbranch_execz .Lagg_invalid
	v_bfe_u32 v4, v0, 2, 4
	v_lshlrev_b32_e32 v53, 4, v3
	v_or_b32_e32 v10, v53, v4
	v_and_b32_e32 v54, 48, v2
	v_lshl_or_b32 v11, v10, 7, v54
	global_load_dwordx4 v[2:5], v11, s[4:5]
	global_load_dwordx4 v[6:9], v11, s[4:5] offset:64
	v_ashrrev_i32_e32 v11, 31, v10
	v_lshl_add_u64 v[10:11], v[10:11], 2, s[6:7]
	global_load_dwordx2 v[50:51], v[10:11], off
	s_waitcnt vmcnt(3)
	ds_write_b128 v98, v[64:67]
	ds_write_b128 v98, v[68:71] offset:4096
	ds_write_b128 v98, v[72:75] offset:8192
	ds_write_b128 v98, v[76:79] offset:12288
	ds_write_b128 v98, v[80:83] offset:16384
	ds_write_b128 v98, v[84:87] offset:20480
	ds_write_b128 v98, v[88:91] offset:24576
	ds_write_b128 v98, v[92:95] offset:28672
	s_waitcnt vmcnt(2)
	v_cvt_pk_f32_fp8_e32 v[10:11], v2
	v_cvt_pk_f32_fp8_sdwa v[12:13], v2 src0_sel:WORD_1
	v_cvt_pk_f32_fp8_e32 v[14:15], v3
	v_cvt_pk_f32_fp8_sdwa v[2:3], v3 src0_sel:WORD_1
	v_cvt_pk_f32_fp8_e32 v[16:17], v4
	v_cvt_pk_f32_fp8_sdwa v[18:19], v4 src0_sel:WORD_1
	v_cvt_pk_f32_fp8_e32 v[20:21], v5
	v_cvt_pk_f32_fp8_sdwa v[4:5], v5 src0_sel:WORD_1
	s_waitcnt vmcnt(1)
	v_cvt_pk_f32_fp8_e32 v[22:23], v6
	v_cvt_pk_f32_fp8_sdwa v[24:25], v6 src0_sel:WORD_1
	v_cvt_pk_f32_fp8_e32 v[26:27], v7
	v_cvt_pk_f32_fp8_sdwa v[6:7], v7 src0_sel:WORD_1
	v_cvt_pk_f32_fp8_e32 v[28:29], v8
	v_cvt_pk_f32_fp8_sdwa v[30:31], v8 src0_sel:WORD_1
	v_cvt_pk_f32_fp8_e32 v[32:33], v9
	v_cvt_pk_f32_fp8_sdwa v[8:9], v9 src0_sel:WORD_1
	v_add_f32_e32 v88, 0, v10
	v_add_f32_e32 v89, 0, v11
	v_add_f32_e32 v90, 0, v12
	v_add_f32_e32 v91, 0, v13
	v_add_f32_e32 v92, 0, v14
	v_add_f32_e32 v93, 0, v15
	v_add_f32_e32 v94, 0, v2
	v_add_f32_e32 v95, 0, v3
	v_add_f32_e32 v76, 0, v16
	v_add_f32_e32 v77, 0, v17
	v_add_f32_e32 v80, 0, v18
	v_add_f32_e32 v81, 0, v19
	v_add_f32_e32 v84, 0, v20
	v_add_f32_e32 v85, 0, v21
	v_add_f32_e32 v86, 0, v4
	v_add_f32_e32 v87, 0, v5
	v_add_f32_e32 v72, 0, v22
	v_add_f32_e32 v73, 0, v23
	v_add_f32_e32 v74, 0, v24
	v_add_f32_e32 v75, 0, v25
	v_add_f32_e32 v78, 0, v26
	v_add_f32_e32 v79, 0, v27
	v_add_f32_e32 v82, 0, v6
	v_add_f32_e32 v83, 0, v7
	v_add_f32_e32 v64, 0, v28
	v_add_f32_e32 v65, 0, v29
	v_add_f32_e32 v66, 0, v30
	v_add_f32_e32 v67, 0, v31
	v_add_f32_e32 v68, 0, v32
	v_add_f32_e32 v69, 0, v33
	v_add_f32_e32 v70, 0, v8
	v_add_f32_e32 v71, 0, v9
	s_waitcnt vmcnt(0)
	s_mov_b64 s[6:7], exec
	v_add_u32_e32 v55, -1, v51
	v_max_i32_e32 v55, 0, v55
	v_mov_b32_e32 v62, 0xc35000
	v_add_u32_e32 v104, 0, v50
	v_min_i32_e32 v104, v104, v55
	v_lshlrev_b32_e32 v104, 2, v104
	global_load_dword v56, v104, s[8:9]
	v_add_u32_e32 v104, 1, v50
	v_min_i32_e32 v104, v104, v55
	v_lshlrev_b32_e32 v104, 2, v104
	global_load_dword v57, v104, s[8:9]
	v_add_u32_e32 v104, 2, v50
	v_min_i32_e32 v104, v104, v55
	v_lshlrev_b32_e32 v104, 2, v104
	global_load_dword v58, v104, s[8:9]
	v_add_u32_e32 v104, 3, v50
	v_min_i32_e32 v104, v104, v55
	v_lshlrev_b32_e32 v104, 2, v104
	global_load_dword v59, v104, s[8:9]
	v_add_u32_e32 v104, 4, v50
	v_min_i32_e32 v104, v104, v55
	v_lshlrev_b32_e32 v104, 2, v104
	global_load_dword v60, v104, s[8:9]
	v_add_u32_e32 v104, 5, v50
	v_min_i32_e32 v104, v104, v55
	v_lshlrev_b32_e32 v104, 2, v104
	global_load_dword v61, v104, s[8:9]
	s_waitcnt vmcnt(0)
	v_add_u32_e32 v104, 0, v50
	v_cmp_lt_i32_e32 vcc, v104, v51
	v_lshlrev_b32_e32 v105, 7, v56
	v_add_u32_e32 v106, 6, v104
	v_min_i32_e32 v106, v106, v55
	v_cndmask_b32_e32 v105, v62, v105, vcc
	v_or_b32_e32 v105, v54, v105
	global_load_dwordx4 v[2:5], v105, s[4:5]
	global_load_dwordx4 v[6:9], v105, s[4:5] offset:64
	v_lshlrev_b32_e32 v106, 2, v106
	global_load_dword v56, v106, s[8:9]
	v_add_u32_e32 v104, 1, v50
	v_cmp_lt_i32_e32 vcc, v104, v51
	v_lshlrev_b32_e32 v105, 7, v57
	v_add_u32_e32 v106, 6, v104
	v_min_i32_e32 v106, v106, v55
	v_cndmask_b32_e32 v105, v62, v105, vcc
	v_or_b32_e32 v105, v54, v105
	global_load_dwordx4 v[10:13], v105, s[4:5]
	global_load_dwordx4 v[14:17], v105, s[4:5] offset:64
	v_lshlrev_b32_e32 v106, 2, v106
	global_load_dword v57, v106, s[8:9]
	v_add_u32_e32 v104, 2, v50
	v_cmp_lt_i32_e32 vcc, v104, v51
	v_lshlrev_b32_e32 v105, 7, v58
	v_add_u32_e32 v106, 6, v104
	v_min_i32_e32 v106, v106, v55
	v_cndmask_b32_e32 v105, v62, v105, vcc
	v_or_b32_e32 v105, v54, v105
	global_load_dwordx4 v[18:21], v105, s[4:5]
	global_load_dwordx4 v[22:25], v105, s[4:5] offset:64
	v_lshlrev_b32_e32 v106, 2, v106
	global_load_dword v58, v106, s[8:9]
	v_add_u32_e32 v104, 3, v50
	v_cmp_lt_i32_e32 vcc, v104, v51
	v_lshlrev_b32_e32 v105, 7, v59
	v_add_u32_e32 v106, 6, v104
	v_min_i32_e32 v106, v106, v55
	v_cndmask_b32_e32 v105, v62, v105, vcc
	v_or_b32_e32 v105, v54, v105
	global_load_dwordx4 v[26:29], v105, s[4:5]
	global_load_dwordx4 v[30:33], v105, s[4:5] offset:64
	v_lshlrev_b32_e32 v106, 2, v106
	global_load_dword v59, v106, s[8:9]
	v_add_u32_e32 v104, 4, v50
	v_cmp_lt_i32_e32 vcc, v104, v51
	v_lshlrev_b32_e32 v105, 7, v60
	v_add_u32_e32 v106, 6, v104
	v_min_i32_e32 v106, v106, v55
	v_cndmask_b32_e32 v105, v62, v105, vcc
	v_or_b32_e32 v105, v54, v105
	global_load_dwordx4 v[34:37], v105, s[4:5]
	global_load_dwordx4 v[38:41], v105, s[4:5] offset:64
	v_lshlrev_b32_e32 v106, 2, v106
	global_load_dword v60, v106, s[8:9]
	v_add_u32_e32 v104, 5, v50
	v_cmp_lt_i32_e32 vcc, v104, v51
	v_lshlrev_b32_e32 v105, 7, v61
	v_add_u32_e32 v106, 6, v104
	v_min_i32_e32 v106, v106, v55
	v_cndmask_b32_e32 v105, v62, v105, vcc
	v_or_b32_e32 v105, v54, v105
	global_load_dwordx4 v[42:45], v105, s[4:5]
	global_load_dwordx4 v[46:49], v105, s[4:5] offset:64
	v_lshlrev_b32_e32 v106, 2, v106
	global_load_dword v61, v106, s[8:9]
.Lagg_gloop:
	s_waitcnt vmcnt(15)
	v_cvt_pk_f32_fp8_e32 v[96:97], v2
	v_cvt_pk_f32_fp8_sdwa v[98:99], v2 src0_sel:WORD_1
	v_cvt_pk_f32_fp8_e32 v[100:101], v3
	v_cvt_pk_f32_fp8_sdwa v[102:103], v3 src0_sel:WORD_1
	v_pk_add_f32 v[88:89], v[88:89], v[96:97]
	v_pk_add_f32 v[90:91], v[90:91], v[98:99]
	v_pk_add_f32 v[92:93], v[92:93], v[100:101]
	v_pk_add_f32 v[94:95], v[94:95], v[102:103]
	v_cvt_pk_f32_fp8_e32 v[96:97], v4
	v_cvt_pk_f32_fp8_sdwa v[98:99], v4 src0_sel:WORD_1
	v_cvt_pk_f32_fp8_e32 v[100:101], v5
	v_cvt_pk_f32_fp8_sdwa v[102:103], v5 src0_sel:WORD_1
	v_pk_add_f32 v[76:77], v[76:77], v[96:97]
	v_pk_add_f32 v[80:81], v[80:81], v[98:99]
	v_pk_add_f32 v[84:85], v[84:85], v[100:101]
	v_pk_add_f32 v[86:87], v[86:87], v[102:103]
	v_cvt_pk_f32_fp8_e32 v[96:97], v6
	v_cvt_pk_f32_fp8_sdwa v[98:99], v6 src0_sel:WORD_1
	v_cvt_pk_f32_fp8_e32 v[100:101], v7
	v_cvt_pk_f32_fp8_sdwa v[102:103], v7 src0_sel:WORD_1
	v_pk_add_f32 v[72:73], v[72:73], v[96:97]
	v_pk_add_f32 v[74:75], v[74:75], v[98:99]
	v_pk_add_f32 v[78:79], v[78:79], v[100:101]
	v_pk_add_f32 v[82:83], v[82:83], v[102:103]
	v_cvt_pk_f32_fp8_e32 v[96:97], v8
	v_cvt_pk_f32_fp8_sdwa v[98:99], v8 src0_sel:WORD_1
	v_cvt_pk_f32_fp8_e32 v[100:101], v9
	v_cvt_pk_f32_fp8_sdwa v[102:103], v9 src0_sel:WORD_1
	v_pk_add_f32 v[64:65], v[64:65], v[96:97]
	v_pk_add_f32 v[66:67], v[66:67], v[98:99]
	v_pk_add_f32 v[68:69], v[68:69], v[100:101]
	v_pk_add_f32 v[70:71], v[70:71], v[102:103]
	v_add_u32_e32 v104, 6, v50
	v_cmp_lt_i32_e32 vcc, v104, v51
	v_lshlrev_b32_e32 v105, 7, v56
	v_add_u32_e32 v106, 6, v104
	v_min_i32_e32 v106, v106, v55
	v_cndmask_b32_e32 v105, v62, v105, vcc
	v_or_b32_e32 v105, v54, v105
	global_load_dwordx4 v[2:5], v105, s[4:5]
	global_load_dwordx4 v[6:9], v105, s[4:5] offset:64
	v_lshlrev_b32_e32 v106, 2, v106
	global_load_dword v56, v106, s[8:9]
	s_waitcnt vmcnt(15)
	v_cvt_pk_f32_fp8_e32 v[96:97], v10
	v_cvt_pk_f32_fp8_sdwa v[98:99], v10 src0_sel:WORD_1
	v_cvt_pk_f32_fp8_e32 v[100:101], v11
	v_cvt_pk_f32_fp8_sdwa v[102:103], v11 src0_sel:WORD_1
	v_pk_add_f32 v[88:89], v[88:89], v[96:97]
	v_pk_add_f32 v[90:91], v[90:91], v[98:99]
	v_pk_add_f32 v[92:93], v[92:93], v[100:101]
	v_pk_add_f32 v[94:95], v[94:95], v[102:103]
	v_cvt_pk_f32_fp8_e32 v[96:97], v12
	v_cvt_pk_f32_fp8_sdwa v[98:99], v12 src0_sel:WORD_1
	v_cvt_pk_f32_fp8_e32 v[100:101], v13
	v_cvt_pk_f32_fp8_sdwa v[102:103], v13 src0_sel:WORD_1
	v_pk_add_f32 v[76:77], v[76:77], v[96:97]
	v_pk_add_f32 v[80:81], v[80:81], v[98:99]
	v_pk_add_f32 v[84:85], v[84:85], v[100:101]
	v_pk_add_f32 v[86:87], v[86:87], v[102:103]
	v_cvt_pk_f32_fp8_e32 v[96:97], v14
	v_cvt_pk_f32_fp8_sdwa v[98:99], v14 src0_sel:WORD_1
	v_cvt_pk_f32_fp8_e32 v[100:101], v15
	v_cvt_pk_f32_fp8_sdwa v[102:103], v15 src0_sel:WORD_1
	v_pk_add_f32 v[72:73], v[72:73], v[96:97]
	v_pk_add_f32 v[74:75], v[74:75], v[98:99]
	v_pk_add_f32 v[78:79], v[78:79], v[100:101]
	v_pk_add_f32 v[82:83], v[82:83], v[102:103]
	v_cvt_pk_f32_fp8_e32 v[96:97], v16
	v_cvt_pk_f32_fp8_sdwa v[98:99], v16 src0_sel:WORD_1
	v_cvt_pk_f32_fp8_e32 v[100:101], v17
	v_cvt_pk_f32_fp8_sdwa v[102:103], v17 src0_sel:WORD_1
	v_pk_add_f32 v[64:65], v[64:65], v[96:97]
	v_pk_add_f32 v[66:67], v[66:67], v[98:99]
	v_pk_add_f32 v[68:69], v[68:69], v[100:101]
	v_pk_add_f32 v[70:71], v[70:71], v[102:103]
	v_add_u32_e32 v104, 7, v50
	v_cmp_lt_i32_e32 vcc, v104, v51
	v_lshlrev_b32_e32 v105, 7, v57
	v_add_u32_e32 v106, 6, v104
	v_min_i32_e32 v106, v106, v55
	v_cndmask_b32_e32 v105, v62, v105, vcc
	v_or_b32_e32 v105, v54, v105
	global_load_dwordx4 v[10:13], v105, s[4:5]
	global_load_dwordx4 v[14:17], v105, s[4:5] offset:64
	v_lshlrev_b32_e32 v106, 2, v106
	global_load_dword v57, v106, s[8:9]
	s_waitcnt vmcnt(15)
	v_cvt_pk_f32_fp8_e32 v[96:97], v18
	v_cvt_pk_f32_fp8_sdwa v[98:99], v18 src0_sel:WORD_1
	v_cvt_pk_f32_fp8_e32 v[100:101], v19
	v_cvt_pk_f32_fp8_sdwa v[102:103], v19 src0_sel:WORD_1
	v_pk_add_f32 v[88:89], v[88:89], v[96:97]
	v_pk_add_f32 v[90:91], v[90:91], v[98:99]
	v_pk_add_f32 v[92:93], v[92:93], v[100:101]
	v_pk_add_f32 v[94:95], v[94:95], v[102:103]
	v_cvt_pk_f32_fp8_e32 v[96:97], v20
	v_cvt_pk_f32_fp8_sdwa v[98:99], v20 src0_sel:WORD_1
	v_cvt_pk_f32_fp8_e32 v[100:101], v21
	v_cvt_pk_f32_fp8_sdwa v[102:103], v21 src0_sel:WORD_1
	v_pk_add_f32 v[76:77], v[76:77], v[96:97]
	v_pk_add_f32 v[80:81], v[80:81], v[98:99]
	v_pk_add_f32 v[84:85], v[84:85], v[100:101]
	v_pk_add_f32 v[86:87], v[86:87], v[102:103]
	v_cvt_pk_f32_fp8_e32 v[96:97], v22
	v_cvt_pk_f32_fp8_sdwa v[98:99], v22 src0_sel:WORD_1
	v_cvt_pk_f32_fp8_e32 v[100:101], v23
	v_cvt_pk_f32_fp8_sdwa v[102:103], v23 src0_sel:WORD_1
	v_pk_add_f32 v[72:73], v[72:73], v[96:97]
	v_pk_add_f32 v[74:75], v[74:75], v[98:99]
	v_pk_add_f32 v[78:79], v[78:79], v[100:101]
	v_pk_add_f32 v[82:83], v[82:83], v[102:103]
	v_cvt_pk_f32_fp8_e32 v[96:97], v24
	v_cvt_pk_f32_fp8_sdwa v[98:99], v24 src0_sel:WORD_1
	v_cvt_pk_f32_fp8_e32 v[100:101], v25
	v_cvt_pk_f32_fp8_sdwa v[102:103], v25 src0_sel:WORD_1
	v_pk_add_f32 v[64:65], v[64:65], v[96:97]
	v_pk_add_f32 v[66:67], v[66:67], v[98:99]
	v_pk_add_f32 v[68:69], v[68:69], v[100:101]
	v_pk_add_f32 v[70:71], v[70:71], v[102:103]
	v_add_u32_e32 v104, 8, v50
	v_cmp_lt_i32_e32 vcc, v104, v51
	v_lshlrev_b32_e32 v105, 7, v58
	v_add_u32_e32 v106, 6, v104
	v_min_i32_e32 v106, v106, v55
	v_cndmask_b32_e32 v105, v62, v105, vcc
	v_or_b32_e32 v105, v54, v105
	global_load_dwordx4 v[18:21], v105, s[4:5]
	global_load_dwordx4 v[22:25], v105, s[4:5] offset:64
	v_lshlrev_b32_e32 v106, 2, v106
	global_load_dword v58, v106, s[8:9]
	s_waitcnt vmcnt(15)
	v_cvt_pk_f32_fp8_e32 v[96:97], v26
	v_cvt_pk_f32_fp8_sdwa v[98:99], v26 src0_sel:WORD_1
	v_cvt_pk_f32_fp8_e32 v[100:101], v27
	v_cvt_pk_f32_fp8_sdwa v[102:103], v27 src0_sel:WORD_1
	v_pk_add_f32 v[88:89], v[88:89], v[96:97]
	v_pk_add_f32 v[90:91], v[90:91], v[98:99]
	v_pk_add_f32 v[92:93], v[92:93], v[100:101]
	v_pk_add_f32 v[94:95], v[94:95], v[102:103]
	v_cvt_pk_f32_fp8_e32 v[96:97], v28
	v_cvt_pk_f32_fp8_sdwa v[98:99], v28 src0_sel:WORD_1
	v_cvt_pk_f32_fp8_e32 v[100:101], v29
	v_cvt_pk_f32_fp8_sdwa v[102:103], v29 src0_sel:WORD_1
	v_pk_add_f32 v[76:77], v[76:77], v[96:97]
	v_pk_add_f32 v[80:81], v[80:81], v[98:99]
	v_pk_add_f32 v[84:85], v[84:85], v[100:101]
	v_pk_add_f32 v[86:87], v[86:87], v[102:103]
	v_cvt_pk_f32_fp8_e32 v[96:97], v30
	v_cvt_pk_f32_fp8_sdwa v[98:99], v30 src0_sel:WORD_1
	v_cvt_pk_f32_fp8_e32 v[100:101], v31
	v_cvt_pk_f32_fp8_sdwa v[102:103], v31 src0_sel:WORD_1
	v_pk_add_f32 v[72:73], v[72:73], v[96:97]
	v_pk_add_f32 v[74:75], v[74:75], v[98:99]
	v_pk_add_f32 v[78:79], v[78:79], v[100:101]
	v_pk_add_f32 v[82:83], v[82:83], v[102:103]
	v_cvt_pk_f32_fp8_e32 v[96:97], v32
	v_cvt_pk_f32_fp8_sdwa v[98:99], v32 src0_sel:WORD_1
	v_cvt_pk_f32_fp8_e32 v[100:101], v33
	v_cvt_pk_f32_fp8_sdwa v[102:103], v33 src0_sel:WORD_1
	v_pk_add_f32 v[64:65], v[64:65], v[96:97]
	v_pk_add_f32 v[66:67], v[66:67], v[98:99]
	v_pk_add_f32 v[68:69], v[68:69], v[100:101]
	v_pk_add_f32 v[70:71], v[70:71], v[102:103]
	v_add_u32_e32 v104, 9, v50
	v_cmp_lt_i32_e32 vcc, v104, v51
	v_lshlrev_b32_e32 v105, 7, v59
	v_add_u32_e32 v106, 6, v104
	v_min_i32_e32 v106, v106, v55
	v_cndmask_b32_e32 v105, v62, v105, vcc
	v_or_b32_e32 v105, v54, v105
	global_load_dwordx4 v[26:29], v105, s[4:5]
	global_load_dwordx4 v[30:33], v105, s[4:5] offset:64
	v_lshlrev_b32_e32 v106, 2, v106
	global_load_dword v59, v106, s[8:9]
	s_waitcnt vmcnt(15)
	v_cvt_pk_f32_fp8_e32 v[96:97], v34
	v_cvt_pk_f32_fp8_sdwa v[98:99], v34 src0_sel:WORD_1
	v_cvt_pk_f32_fp8_e32 v[100:101], v35
	v_cvt_pk_f32_fp8_sdwa v[102:103], v35 src0_sel:WORD_1
	v_pk_add_f32 v[88:89], v[88:89], v[96:97]
	v_pk_add_f32 v[90:91], v[90:91], v[98:99]
	v_pk_add_f32 v[92:93], v[92:93], v[100:101]
	v_pk_add_f32 v[94:95], v[94:95], v[102:103]
	v_cvt_pk_f32_fp8_e32 v[96:97], v36
	v_cvt_pk_f32_fp8_sdwa v[98:99], v36 src0_sel:WORD_1
	v_cvt_pk_f32_fp8_e32 v[100:101], v37
	v_cvt_pk_f32_fp8_sdwa v[102:103], v37 src0_sel:WORD_1
	v_pk_add_f32 v[76:77], v[76:77], v[96:97]
	v_pk_add_f32 v[80:81], v[80:81], v[98:99]
	v_pk_add_f32 v[84:85], v[84:85], v[100:101]
	v_pk_add_f32 v[86:87], v[86:87], v[102:103]
	v_cvt_pk_f32_fp8_e32 v[96:97], v38
	v_cvt_pk_f32_fp8_sdwa v[98:99], v38 src0_sel:WORD_1
	v_cvt_pk_f32_fp8_e32 v[100:101], v39
	v_cvt_pk_f32_fp8_sdwa v[102:103], v39 src0_sel:WORD_1
	v_pk_add_f32 v[72:73], v[72:73], v[96:97]
	v_pk_add_f32 v[74:75], v[74:75], v[98:99]
	v_pk_add_f32 v[78:79], v[78:79], v[100:101]
	v_pk_add_f32 v[82:83], v[82:83], v[102:103]
	v_cvt_pk_f32_fp8_e32 v[96:97], v40
	v_cvt_pk_f32_fp8_sdwa v[98:99], v40 src0_sel:WORD_1
	v_cvt_pk_f32_fp8_e32 v[100:101], v41
	v_cvt_pk_f32_fp8_sdwa v[102:103], v41 src0_sel:WORD_1
	v_pk_add_f32 v[64:65], v[64:65], v[96:97]
	v_pk_add_f32 v[66:67], v[66:67], v[98:99]
	v_pk_add_f32 v[68:69], v[68:69], v[100:101]
	v_pk_add_f32 v[70:71], v[70:71], v[102:103]
	v_add_u32_e32 v104, 10, v50
	v_cmp_lt_i32_e32 vcc, v104, v51
	v_lshlrev_b32_e32 v105, 7, v60
	v_add_u32_e32 v106, 6, v104
	v_min_i32_e32 v106, v106, v55
	v_cndmask_b32_e32 v105, v62, v105, vcc
	v_or_b32_e32 v105, v54, v105
	global_load_dwordx4 v[34:37], v105, s[4:5]
	global_load_dwordx4 v[38:41], v105, s[4:5] offset:64
	v_lshlrev_b32_e32 v106, 2, v106
	global_load_dword v60, v106, s[8:9]
	s_waitcnt vmcnt(15)
	v_cvt_pk_f32_fp8_e32 v[96:97], v42
	v_cvt_pk_f32_fp8_sdwa v[98:99], v42 src0_sel:WORD_1
	v_cvt_pk_f32_fp8_e32 v[100:101], v43
	v_cvt_pk_f32_fp8_sdwa v[102:103], v43 src0_sel:WORD_1
	v_pk_add_f32 v[88:89], v[88:89], v[96:97]
	v_pk_add_f32 v[90:91], v[90:91], v[98:99]
	v_pk_add_f32 v[92:93], v[92:93], v[100:101]
	v_pk_add_f32 v[94:95], v[94:95], v[102:103]
	v_cvt_pk_f32_fp8_e32 v[96:97], v44
	v_cvt_pk_f32_fp8_sdwa v[98:99], v44 src0_sel:WORD_1
	v_cvt_pk_f32_fp8_e32 v[100:101], v45
	v_cvt_pk_f32_fp8_sdwa v[102:103], v45 src0_sel:WORD_1
	v_pk_add_f32 v[76:77], v[76:77], v[96:97]
	v_pk_add_f32 v[80:81], v[80:81], v[98:99]
	v_pk_add_f32 v[84:85], v[84:85], v[100:101]
	v_pk_add_f32 v[86:87], v[86:87], v[102:103]
	v_cvt_pk_f32_fp8_e32 v[96:97], v46
	v_cvt_pk_f32_fp8_sdwa v[98:99], v46 src0_sel:WORD_1
	v_cvt_pk_f32_fp8_e32 v[100:101], v47
	v_cvt_pk_f32_fp8_sdwa v[102:103], v47 src0_sel:WORD_1
	v_pk_add_f32 v[72:73], v[72:73], v[96:97]
	v_pk_add_f32 v[74:75], v[74:75], v[98:99]
	v_pk_add_f32 v[78:79], v[78:79], v[100:101]
	v_pk_add_f32 v[82:83], v[82:83], v[102:103]
	v_cvt_pk_f32_fp8_e32 v[96:97], v48
	v_cvt_pk_f32_fp8_sdwa v[98:99], v48 src0_sel:WORD_1
	v_cvt_pk_f32_fp8_e32 v[100:101], v49
	v_cvt_pk_f32_fp8_sdwa v[102:103], v49 src0_sel:WORD_1
	v_pk_add_f32 v[64:65], v[64:65], v[96:97]
	v_pk_add_f32 v[66:67], v[66:67], v[98:99]
	v_pk_add_f32 v[68:69], v[68:69], v[100:101]
	v_pk_add_f32 v[70:71], v[70:71], v[102:103]
	v_add_u32_e32 v104, 11, v50
	v_cmp_lt_i32_e32 vcc, v104, v51
	v_lshlrev_b32_e32 v105, 7, v61
	v_add_u32_e32 v106, 6, v104
	v_min_i32_e32 v106, v106, v55
	v_cndmask_b32_e32 v105, v62, v105, vcc
	v_or_b32_e32 v105, v54, v105
	global_load_dwordx4 v[42:45], v105, s[4:5]
	global_load_dwordx4 v[46:49], v105, s[4:5] offset:64
	v_lshlrev_b32_e32 v106, 2, v106
	global_load_dword v61, v106, s[8:9]
	v_add_u32_e32 v50, 6, v50
	v_cmp_lt_i32_e32 vcc, v50, v51
	s_and_b64 vcc, exec, vcc
	s_cbranch_scc1 .Lagg_gloop
	s_waitcnt vmcnt(0)
.LBB2_7:
	s_or_b64 exec, exec, s[6:7]
	s_waitcnt lgkmcnt(0)
	s_barrier
	v_and_b32_e32 v2, 63, v0
	v_lshrrev_b32_e32 v100, 4, v2
	v_and_or_b32 v3, v1, 60, v100
	v_lshlrev_b32_e32 v101, 2, v3
	v_cvt_pk_f16_f32 v3, v94, v95
	v_cvt_pk_f16_f32 v6, v92, v93
	v_cvt_pk_f16_f32 v5, v90, v91
	v_cvt_pk_f16_f32 v4, v88, v89
	ds_bpermute_b32 v4, v101, v4
	ds_bpermute_b32 v5, v101, v5
	ds_bpermute_b32 v6, v101, v6
	ds_bpermute_b32 v7, v101, v3
	v_lshlrev_b32_e32 v102, 4, v2
	v_cvt_pk_f16_f32 v2, v86, v87
	v_cvt_pk_f16_f32 v3, v84, v85
	s_waitcnt vmcnt(0)
	v_cvt_pk_f16_f32 v62, v80, v81
	v_cvt_pk_f16_f32 v63, v76, v77
	ds_bpermute_b32 v84, v101, v63
	ds_bpermute_b32 v85, v101, v62
	ds_bpermute_b32 v86, v101, v3
	ds_bpermute_b32 v87, v101, v2
	ds_read_b128 v[8:11], v102
	ds_read_b128 v[12:15], v102 offset:1024
	ds_read_b128 v[16:19], v102 offset:4096
	ds_read_b128 v[20:23], v102 offset:8192
	ds_read_b128 v[24:27], v102 offset:5120
	ds_read_b128 v[28:31], v102 offset:12288
	ds_read_b128 v[32:35], v102 offset:9216
	ds_read_b128 v[36:39], v102 offset:16384
	ds_read_b128 v[40:43], v102 offset:13312
	ds_read_b128 v[44:47], v102 offset:20480
	ds_read_b128 v[48:51], v102 offset:17408
	ds_read_b128 v[54:57], v102 offset:24576
	ds_read_b128 v[58:61], v102 offset:21504
	ds_read_b128 v[88:91], v102 offset:28672
	ds_read_b128 v[92:95], v102 offset:25600
	s_waitcnt lgkmcnt(14)
	v_mfma_f32_16x16x32_f16 v[8:11], v[4:7], v[8:11], 0
	v_lshlrev_b32_e32 v2, 3, v0
	v_and_b32_e32 v103, 0x78, v2
	v_lshlrev_b32_e32 v104, 2, v103
	s_waitcnt lgkmcnt(12)
	v_mfma_f32_16x16x32_f16 v[16:19], v[4:7], v[16:19], 0
	v_cvt_pk_f16_f32 v2, v82, v83
	v_cvt_pk_f16_f32 v3, v78, v79
	ds_read_b128 v[96:99], v102 offset:29696
	s_waitcnt lgkmcnt(12)
	v_mfma_f32_16x16x32_f16 v[20:23], v[4:7], v[20:23], 0
	v_cvt_pk_f16_f32 v66, v66, v67
	v_cvt_pk_f16_f32 v67, v64, v65
	s_waitcnt lgkmcnt(10)
	v_mfma_f32_16x16x32_f16 v[28:31], v[4:7], v[28:31], 0
	s_waitcnt lgkmcnt(8)
	v_mfma_f32_16x16x32_f16 v[36:39], v[4:7], v[36:39], 0
	s_waitcnt lgkmcnt(6)
	v_mfma_f32_16x16x32_f16 v[44:47], v[4:7], v[44:47], 0
	s_waitcnt lgkmcnt(4)
	v_mfma_f32_16x16x32_f16 v[54:57], v[4:7], v[54:57], 0
	s_waitcnt lgkmcnt(2)
	v_mfma_f32_16x16x32_f16 v[88:91], v[4:7], v[88:91], 0
	v_cvt_pk_f16_f32 v4, v74, v75
	v_cvt_pk_f16_f32 v5, v72, v73
	v_mfma_f32_16x16x32_f16 v[10:13], v[84:87], v[12:15], v[8:11]
	v_mfma_f32_16x16x32_f16 v[14:17], v[84:87], v[24:27], v[16:19]
	s_nop 1
	global_load_dwordx4 v[6:9], v104, s[12:13] offset:16
	v_mfma_f32_16x16x32_f16 v[18:21], v[84:87], v[32:35], v[20:23]
	ds_bpermute_b32 v32, v101, v3
	ds_bpermute_b32 v33, v101, v2
	v_mfma_f32_16x16x32_f16 v[22:25], v[84:87], v[40:43], v[28:31]
	s_nop 2
	ds_bpermute_b32 v30, v101, v5
	ds_bpermute_b32 v31, v101, v4
	global_load_dwordx4 v[2:5], v104, s[12:13]
	v_mfma_f32_16x16x32_f16 v[26:29], v[84:87], v[48:51], v[36:39]
	v_cvt_pk_f16_f32 v50, v70, v71
	v_cvt_pk_f16_f32 v51, v68, v69
	v_mfma_f32_16x16x32_f16 v[34:37], v[84:87], v[58:61], v[44:47]
	s_nop 2
	ds_read_b128 v[46:49], v102 offset:2048
	s_waitcnt lgkmcnt(6)
	v_mfma_f32_16x16x32_f16 v[38:41], v[84:87], v[92:95], v[54:57]
	s_nop 2
	ds_read_b128 v[54:57], v102 offset:3072
	s_waitcnt lgkmcnt(1)
	v_mfma_f32_16x16x32_f16 v[10:13], v[30:33], v[46:49], v[10:13]
	ds_read_b128 v[46:49], v102 offset:6144
	ds_read_b128 v[58:61], v102 offset:10240
	ds_read_b128 v[72:75], v102 offset:7168
	s_waitcnt lgkmcnt(2)
	v_mfma_f32_16x16x32_f16 v[14:17], v[30:33], v[46:49], v[14:17]
	ds_read_b128 v[46:49], v102 offset:14336
	ds_read_b128 v[76:79], v102 offset:11264
	s_waitcnt lgkmcnt(3)
	v_mfma_f32_16x16x32_f16 v[18:21], v[30:33], v[58:61], v[18:21]
	ds_read_b128 v[58:61], v102 offset:18432
	ds_read_b128 v[68:71], v102 offset:15360
	s_waitcnt lgkmcnt(3)
	v_mfma_f32_16x16x32_f16 v[22:25], v[30:33], v[46:49], v[22:25]
	ds_read_b128 v[46:49], v102 offset:22528
	ds_read_b128 v[80:83], v102 offset:19456
	s_waitcnt lgkmcnt(1)
	v_mfma_f32_16x16x32_f16 v[34:37], v[30:33], v[46:49], v[34:37]
	ds_bpermute_b32 v46, v101, v67
	ds_bpermute_b32 v47, v101, v66
	ds_bpermute_b32 v48, v101, v51
	ds_bpermute_b32 v49, v101, v50
	v_mfma_f32_16x16x32_f16 v[26:29], v[30:33], v[58:61], v[26:29]
	ds_read_b128 v[58:61], v102 offset:26624
	ds_read_b128 v[62:65], v102 offset:23552
	v_mfma_f32_16x16x32_f16 v[42:45], v[84:87], v[96:99], v[88:91]
	ds_read_b128 v[84:87], v102 offset:30720
	s_nop 1
	ds_read_b128 v[88:91], v102 offset:27648
	s_waitcnt lgkmcnt(3)
	v_mfma_f32_16x16x32_f16 v[38:41], v[30:33], v[58:61], v[38:41]
	ds_read_b128 v[58:61], v102 offset:31744
	s_waitcnt lgkmcnt(2)
	v_mfma_f32_16x16x32_f16 v[30:33], v[30:33], v[84:87], v[42:45]
	v_lshlrev_b32_e32 v85, 2, v100
	v_lshlrev_b32_e32 v84, 10, v52
	v_or_b32_e32 v66, v53, v85
	v_lshlrev_b32_e32 v42, 1, v103
	v_mov_b32_e32 v43, 0
	v_mfma_f32_16x16x32_f16 v[14:17], v[46:49], v[72:75], v[14:17]
	v_lshl_add_u64 v[72:73], s[14:15], 0, v[42:43]
	v_ashrrev_i32_e32 v67, 31, v66
	v_mfma_f32_16x16x32_f16 v[42:45], v[46:49], v[76:79], v[18:21]
	v_mfma_f32_16x16x32_f16 v[50:53], v[46:49], v[68:71], v[22:25]
	s_nop 3
	v_mov_b32_e32 v21, v14
	v_lshlrev_b64 v[18:19], 8, v[66:67]
	v_lshl_add_u64 v[74:75], v[72:73], 0, v[18:19]
	v_mfma_f32_16x16x32_f16 v[10:13], v[46:49], v[54:57], v[10:13]
	v_mov_b32_e32 v22, v42
	v_mov_b32_e32 v23, v50
	v_mov_b32_e32 v42, v15
	v_mfma_f32_16x16x32_f16 v[54:57], v[46:49], v[80:83], v[26:29]
	v_or_b32_e32 v18, 1, v66
	s_nop 2
	v_mov_b32_e32 v20, v10
	v_ashrrev_i32_e32 v19, 31, v18
	v_mfma_f32_16x16x32_f16 v[34:37], v[46:49], v[62:65], v[34:37]
	v_lshlrev_b64 v[18:19], 8, v[18:19]
	v_lshl_add_u64 v[68:69], v[72:73], 0, v[18:19]
	v_or_b32_e32 v18, 2, v66
	s_waitcnt lgkmcnt(1)
	v_mfma_f32_16x16x32_f16 v[38:41], v[46:49], v[88:91], v[38:41]
	s_waitcnt vmcnt(0)
	v_pk_add_f32 v[24:25], v[4:5], v[22:23]
	v_mov_b32_e32 v22, v54
	v_mov_b32_e32 v23, v34
	s_waitcnt lgkmcnt(0)
	v_mfma_f32_16x16x32_f16 v[28:31], v[46:49], v[58:61], v[30:33]
	v_add_f32_e64 v26, v6, v22
	v_add_f32_e64 v27, v7, v23
	v_mov_b32_e32 v22, v38
	v_pk_add_f32 v[20:21], v[2:3], v[20:21]
	v_add_f32_e32 v50, v2, v11
	v_cvt_pk_f16_f32 v46, v20, v21
	s_nop 1
	v_mov_b32_e32 v23, v28
	v_pk_add_f32 v[22:23], v[8:9], v[22:23]
	v_cvt_pk_f16_f32 v47, v24, v25
	v_cvt_pk_f16_f32 v48, v26, v27
	v_cvt_pk_f16_f32 v49, v22, v23
	v_cvt_f16_f32_e32 v14, v50
	global_store_dwordx4 v[74:75], v[46:49], off sc0 sc1
	v_mov_b32_e32 v54, v51
	v_add_f32_e32 v51, v9, v29
	v_pk_mov_b32 v[46:47], v[2:3], v[4:5] op_sel:[1,0]
	v_pk_mov_b32 v[48:49], v[6:7], v[8:9] op_sel:[1,0]
	v_pk_add_f32 v[10:11], v[46:47], v[42:43]
	v_mov_b32_e32 v38, v35
	v_cvt_pk_f16_f32 v3, v10, v11
	v_pack_b32_f16 v32, v14, v3
	v_pk_mov_b32 v[14:15], v[4:5], v[6:7] op_sel:[1,0]
	v_pk_add_f32 v[28:29], v[48:49], v[38:39]
	v_pk_add_f32 v[42:43], v[14:15], v[54:55]
	v_cvt_pk_f16_f32 v5, v28, v29
	v_cvt_pk_f16_f32 v4, v42, v43
	v_alignbit_b32 v33, v4, v3, 16
	v_cvt_f16_f32_e32 v3, v51
	v_alignbit_b32 v34, v5, v4, 16
	v_add_f32_e32 v54, v2, v12
	v_mov_b32_e32 v6, v52
	v_alignbit_b32 v35, v3, v5, 16
	v_mov_b32_e32 v7, v56
	global_store_dwordx4 v[68:69], v[32:35], off sc0 sc1
	v_cvt_f16_f32_e32 v3, v54
	v_mov_b32_e32 v4, v16
	v_pk_add_f32 v[34:35], v[14:15], v[6:7]
	v_mov_b32_e32 v6, v36
	v_add_f32_e32 v36, v9, v30
	v_mov_b32_e32 v5, v44
	v_cvt_f16_f32_e32 v8, v36
	v_add_f32_e32 v52, v2, v13
	v_pk_add_f32 v[32:33], v[46:47], v[4:5]
	v_mov_b32_e32 v7, v40
	v_cvt_f16_f32_e32 v2, v52
	v_ashrrev_i32_e32 v19, 31, v18
	v_cvt_pk_f16_f32 v5, v32, v33
	v_pk_add_f32 v[38:39], v[48:49], v[6:7]
	v_mov_b32_e32 v44, v17
	v_lshlrev_b64 v[18:19], 8, v[18:19]
	v_pack_b32_f16 v4, v3, v5
	v_cvt_pk_f16_f32 v3, v34, v35
	v_cvt_pk_f16_f32 v7, v38, v39
	v_pk_add_f32 v[12:13], v[46:47], v[44:45]
	v_mov_b32_e32 v56, v53
	v_mov_b32_e32 v40, v37
	v_lshl_add_u64 v[62:63], v[72:73], 0, v[18:19]
	v_alignbit_b32 v5, v3, v5, 16
	v_alignbit_b32 v6, v7, v3, 16
	v_alignbit_b32 v7, v8, v7, 16
	v_cvt_pk_f16_f32 v3, v12, v13
	v_pk_add_f32 v[14:15], v[14:15], v[56:57]
	v_pk_add_f32 v[16:17], v[48:49], v[40:41]
	global_store_dwordx4 v[62:63], v[4:7], off sc0 sc1
	v_cvt_pk_f16_f32 v37, v16, v17
	v_add_f32_e32 v9, v9, v31
	v_pack_b32_f16 v6, v2, v3
	v_cvt_pk_f16_f32 v2, v14, v15
	v_alignbit_b32 v7, v2, v3, 16
	v_alignbit_b32 v8, v37, v2, 16
	v_pk_mul_f32 v[2:3], v[22:23], v[22:23]
	v_or_b32_e32 v18, 3, v66
	v_mul_f32_e32 v2, v29, v29
	v_pk_fma_f32 v[4:5], v[22:23], v[22:23], v[2:3] op_sel_hi:[1,1,0]
	v_mul_f32_e32 v2, v39, v39
	v_pk_add_f32 v[4:5], v[2:3], v[4:5] op_sel_hi:[0,1]
	v_mul_f32_e32 v2, v17, v17
	v_pk_add_f32 v[4:5], v[2:3], v[4:5] op_sel_hi:[0,1]
	v_add_f32_e32 v2, 0, v22
	v_add_f32_e32 v2, v29, v2
	v_add_f32_e32 v2, v39, v2
	v_add_f32_e32 v5, v17, v2
	v_mul_f32_e32 v2, v27, v27
	v_pk_fma_f32 v[30:31], v[28:29], v[28:29], v[2:3] op_sel_hi:[1,1,0]
	v_add_f32_e32 v2, 0, v27
	v_add_f32_e32 v2, v28, v2
	v_add_f32_e32 v2, v38, v2
	v_pk_fma_f32 v[30:31], v[38:39], v[38:39], v[30:31]
	v_add_f32_e32 v22, v16, v2
	v_mul_f32_e32 v2, v43, v43
	v_pk_fma_f32 v[30:31], v[16:17], v[16:17], v[30:31]
	v_pk_fma_f32 v[16:17], v[26:27], v[26:27], v[2:3] op_sel_hi:[1,1,0]
	v_mul_f32_e32 v2, v35, v35
	v_pk_add_f32 v[16:17], v[2:3], v[16:17] op_sel_hi:[0,1]
	v_mul_f32_e32 v2, v15, v15
	v_pk_add_f32 v[16:17], v[2:3], v[16:17] op_sel_hi:[0,1]
	v_add_f32_e32 v2, 0, v26
	v_add_f32_e32 v2, v43, v2
	v_add_f32_e32 v2, v35, v2
	v_add_f32_e32 v17, v15, v2
	v_mul_f32_e32 v2, v25, v25
	v_pk_fma_f32 v[26:27], v[42:43], v[42:43], v[2:3] op_sel_hi:[1,1,0]
	v_add_f32_e32 v2, 0, v25
	v_pk_fma_f32 v[26:27], v[34:35], v[34:35], v[26:27]
	v_add_f32_e32 v2, v42, v2
	v_pk_fma_f32 v[26:27], v[14:15], v[14:15], v[26:27]
	v_add_f32_e32 v2, v34, v2
	v_add_f32_e32 v27, v14, v2
	v_mul_f32_e32 v2, v11, v11
	v_pk_fma_f32 v[14:15], v[24:25], v[24:25], v[2:3] op_sel_hi:[1,1,0]
	v_mul_f32_e32 v2, v33, v33
	v_pk_add_f32 v[14:15], v[2:3], v[14:15] op_sel_hi:[0,1]
	v_mul_f32_e32 v2, v13, v13
	v_pk_add_f32 v[14:15], v[2:3], v[14:15] op_sel_hi:[0,1]
	v_add_f32_e32 v2, 0, v24
	v_pk_mul_f32 v[24:25], v[20:21], v[20:21]
	v_add_f32_e32 v2, v11, v2
	v_pk_fma_f32 v[28:29], v[10:11], v[10:11], v[24:25] op_sel:[0,0,1] op_sel_hi:[1,1,0]
	v_add_f32_e32 v11, 0, v21
	v_add_f32_e32 v2, v33, v2
	v_pk_fma_f32 v[28:29], v[32:33], v[32:33], v[28:29]
	v_add_f32_e32 v10, v10, v11
	v_add_f32_e32 v2, v13, v2
	v_pk_fma_f32 v[28:29], v[12:13], v[12:13], v[28:29]
	v_add_f32_e32 v10, v32, v10
	v_add_f32_e32 v11, 0, v20
	v_cvt_f16_f32_e32 v13, v9
	v_add_f32_e32 v10, v12, v10
	v_add_f32_e32 v11, v50, v11
	v_add_f32_e32 v12, 0, v23
	v_ashrrev_i32_e32 v19, 31, v18
	v_add_f32_e32 v11, v54, v11
	v_fmac_f32_e32 v3, v51, v51
	v_add_f32_e32 v12, v51, v12
	v_lshlrev_b64 v[18:19], 8, v[18:19]
	v_add_f32_e32 v11, v52, v11
	v_fmac_f32_e32 v3, v36, v36
	v_add_f32_e32 v12, v36, v12
	v_lshl_add_u64 v[18:19], v[72:73], 0, v[18:19]
	v_add_f32_e32 v12, v9, v12
	v_fmac_f32_e32 v3, v9, v9
	v_alignbit_b32 v9, v13, v37, 16
	v_permlane16_swap_b32_e32 v11, v10
	v_permlane16_swap_b32_e32 v2, v27
	global_store_dwordx4 v[18:19], v[6:9], off sc0 sc1
	v_add_f32_e32 v2, v2, v27
	v_fmac_f32_e32 v24, v50, v50
	v_add_f32_e32 v6, v11, v10
	s_nop 1
	v_permlane32_swap_b32_e32 v6, v2
	v_permlane16_swap_b32_e32 v17, v22
	v_permlane16_swap_b32_e32 v5, v12
	v_fmac_f32_e32 v24, v54, v54
	v_add_f32_e32 v2, v6, v2
	v_add_f32_e32 v6, v17, v22
	v_add_f32_e32 v5, v5, v12
	v_or3_b32 v64, v84, v104, v85
	v_fmac_f32_e32 v24, v52, v52
	v_permlane32_swap_b32_e32 v6, v5
	v_add_f32_e32 v5, v6, v5
	v_add_u32_e32 v6, 0x8000, v64
	v_permlane16_swap_b32_e32 v24, v28
	v_permlane16_swap_b32_e32 v14, v26
	ds_write2_b32 v6, v2, v5 offset1:4
	v_add_f32_e32 v2, v24, v28
	v_add_f32_e32 v5, v14, v26
	s_nop 1
	v_permlane32_swap_b32_e32 v2, v5
	v_permlane16_swap_b32_e32 v16, v30
	v_permlane16_swap_b32_e32 v4, v3
	v_add_f32_e32 v2, v2, v5
	v_add_f32_e32 v5, v16, v30
	v_add_f32_e32 v3, v4, v3
	s_nop 1
	v_permlane32_swap_b32_e32 v5, v3
	v_add_f32_e32 v3, v5, v3
	ds_write2_b32 v6, v2, v3 offset0:128 offset1:132

	.amdhsa_kernel _Z5k_aggPKDF16_PKhPKiS4_PKDv8_DF16_PKfPDF16_Pf
		.amdhsa_group_segment_fixed_size 36864
		.amdhsa_private_segment_fixed_size 0
		.amdhsa_kernarg_size 320
		.amdhsa_user_sgpr_count 2
		.amdhsa_user_sgpr_dispatch_ptr 0
		.amdhsa_user_sgpr_queue_ptr 0
		.amdhsa_user_sgpr_kernarg_segment_ptr 1
		.amdhsa_user_sgpr_dispatch_id 0
		.amdhsa_user_sgpr_kernarg_preload_length 0
		.amdhsa_user_sgpr_kernarg_preload_offset 0
		.amdhsa_user_sgpr_private_segment_size 0
		.amdhsa_uses_dynamic_stack 0
		.amdhsa_enable_private_segment 0
		.amdhsa_system_sgpr_workgroup_id_x 1
		.amdhsa_system_sgpr_workgroup_id_y 0
		.amdhsa_system_sgpr_workgroup_id_z 0
		.amdhsa_system_sgpr_workgroup_info 0
		.amdhsa_system_vgpr_workitem_id 0
		.amdhsa_next_free_vgpr 108
		.amdhsa_next_free_sgpr 96
		.amdhsa_accum_offset 108
		.amdhsa_reserve_vcc 1
		.amdhsa_float_round_mode_32 0
		.amdhsa_float_round_mode_16_64 0
		.amdhsa_float_denorm_mode_32 3
		.amdhsa_float_denorm_mode_16_64 3
		.amdhsa_dx10_clamp 1
		.amdhsa_ieee_mode 1
		.amdhsa_fp16_overflow 0
		.amdhsa_tg_split 0
		.amdhsa_exception_fp_ieee_invalid_op 0
		.amdhsa_exception_fp_denorm_src 0
		.amdhsa_exception_fp_ieee_div_zero 0
		.amdhsa_exception_fp_ieee_overflow 0
		.amdhsa_exception_fp_ieee_underflow 0
		.amdhsa_exception_fp_ieee_inexact 0
		.amdhsa_exception_int_div_zero 0
	.end_amdhsa_kernel

.LBB4_10:
	s_or_b64 exec, exec, s[4:5]
	s_waitcnt vmcnt(0)
	ds_write_b128 v72, v[52:55]
	ds_write_b128 v72, v[56:59] offset:8192
	ds_write_b128 v72, v[64:67] offset:16384
	ds_write_b128 v72, v[68:71] offset:24576
	s_waitcnt lgkmcnt(0)
	s_barrier
	s_and_saveexec_b64 s[0:1], vcc
	s_cbranch_execz .LBB4_12
	v_lshlrev_b32_e32 v19, 5, v23
	ds_read_b128 v[24:27], v19 offset:40960
	ds_read_b128 v[28:31], v19 offset:40976
	ds_read_b128 v[32:35], v19 offset:41472
	v_lshrrev_b32_e32 v64, 4, v22
	v_and_or_b32 v18, v18, 60, v64
	v_lshlrev_b32_e32 v18, 2, v18
	v_lshlrev_b32_e32 v65, 4, v22
	s_waitcnt lgkmcnt(0)
	v_fma_mix_f32 v20, v24, v14, v32 op_sel_hi:[0,1,0]
	v_fma_mix_f32 v14, v25, v14, v33 op_sel:[0,1,0] op_sel_hi:[0,1,0]
	v_fma_mix_f32 v21, v26, v15, v34 op_sel_hi:[0,1,0]
	v_fma_mix_f32 v15, v27, v15, v35 op_sel:[0,1,0] op_sel_hi:[0,1,0]
	ds_read_b128 v[24:27], v19 offset:41488
	v_max_f32_e32 v20, 0, v20
	v_max_f32_e32 v14, 0, v14
	v_max_f32_e32 v21, 0, v21
	v_max_f32_e32 v15, 0, v15
	s_waitcnt lgkmcnt(0)
	v_fma_mix_f32 v23, v28, v16, v24 op_sel_hi:[0,1,0]
	v_fma_mix_f32 v24, v30, v17, v26 op_sel_hi:[0,1,0]
	v_fma_mix_f32 v17, v31, v17, v27 op_sel:[0,1,0] op_sel_hi:[0,1,0]
	v_max_f32_e32 v24, 0, v24
	v_max_f32_e32 v17, 0, v17
	v_fma_mix_f32 v16, v29, v16, v25 op_sel:[0,1,0] op_sel_hi:[0,1,0]
	v_cvt_pk_f16_f32 v17, v24, v17
	ds_read_b128 v[24:27], v19 offset:41088
	ds_read_b128 v[28:31], v19 offset:41600
	v_cvt_pk_f16_f32 v15, v21, v15
	v_cvt_pk_f16_f32 v14, v20, v14
	v_max_f32_e32 v23, 0, v23
	v_max_f32_e32 v16, 0, v16
	s_waitcnt lgkmcnt(0)
	v_fma_mix_f32 v20, v24, v6, v28 op_sel_hi:[0,1,0]
	v_fma_mix_f32 v6, v25, v6, v29 op_sel:[0,1,0] op_sel_hi:[0,1,0]
	v_fma_mix_f32 v21, v26, v7, v30 op_sel_hi:[0,1,0]
	v_fma_mix_f32 v7, v27, v7, v31 op_sel:[0,1,0] op_sel_hi:[0,1,0]
	ds_read_b128 v[24:27], v19 offset:41104
	ds_read_b128 v[28:31], v19 offset:41616
	v_cvt_pk_f16_f32 v16, v23, v16
	v_max_f32_e32 v20, 0, v20
	v_max_f32_e32 v6, 0, v6
	v_max_f32_e32 v21, 0, v21
	s_waitcnt lgkmcnt(0)
	v_fma_mix_f32 v23, v24, v8, v28 op_sel_hi:[0,1,0]
	v_fma_mix_f32 v24, v26, v9, v30 op_sel_hi:[0,1,0]
	v_fma_mix_f32 v9, v27, v9, v31 op_sel:[0,1,0] op_sel_hi:[0,1,0]
	v_max_f32_e32 v24, 0, v24
	v_max_f32_e32 v9, 0, v9
	v_fma_mix_f32 v8, v25, v8, v29 op_sel:[0,1,0] op_sel_hi:[0,1,0]
	v_cvt_pk_f16_f32 v9, v24, v9
	ds_read_b128 v[24:27], v19 offset:41216
	ds_read_b128 v[28:31], v19 offset:41728
	v_max_f32_e32 v7, 0, v7
	v_cvt_pk_f16_f32 v7, v21, v7
	v_cvt_pk_f16_f32 v6, v20, v6
	v_max_f32_e32 v23, 0, v23
	s_waitcnt lgkmcnt(0)
	v_fma_mix_f32 v20, v24, v10, v28 op_sel_hi:[0,1,0]
	v_fma_mix_f32 v10, v25, v10, v29 op_sel:[0,1,0] op_sel_hi:[0,1,0]
	v_fma_mix_f32 v21, v26, v11, v30 op_sel_hi:[0,1,0]
	v_fma_mix_f32 v11, v27, v11, v31 op_sel:[0,1,0] op_sel_hi:[0,1,0]
	ds_read_b128 v[24:27], v19 offset:41232
	ds_read_b128 v[28:31], v19 offset:41744
	v_max_f32_e32 v8, 0, v8
	v_cvt_pk_f16_f32 v8, v23, v8
	v_max_f32_e32 v20, 0, v20
	v_max_f32_e32 v10, 0, v10
	s_waitcnt lgkmcnt(0)
	v_fma_mix_f32 v23, v24, v12, v28 op_sel_hi:[0,1,0]
	v_fma_mix_f32 v24, v26, v13, v30 op_sel_hi:[0,1,0]
	v_fma_mix_f32 v13, v27, v13, v31 op_sel:[0,1,0] op_sel_hi:[0,1,0]
	v_max_f32_e32 v24, 0, v24
	v_max_f32_e32 v13, 0, v13
	v_fma_mix_f32 v12, v25, v12, v29 op_sel:[0,1,0] op_sel_hi:[0,1,0]
	v_cvt_pk_f16_f32 v13, v24, v13
	ds_read_b128 v[24:27], v19 offset:41344
	ds_read_b128 v[28:31], v19 offset:41856
	v_max_f32_e32 v21, 0, v21
	v_max_f32_e32 v11, 0, v11
	v_cvt_pk_f16_f32 v11, v21, v11
	v_cvt_pk_f16_f32 v10, v20, v10
	s_waitcnt lgkmcnt(0)
	v_fma_mix_f32 v20, v24, v2, v28 op_sel_hi:[0,1,0]
	v_fma_mix_f32 v2, v25, v2, v29 op_sel:[0,1,0] op_sel_hi:[0,1,0]
	v_fma_mix_f32 v21, v26, v3, v30 op_sel_hi:[0,1,0]
	v_fma_mix_f32 v3, v27, v3, v31 op_sel:[0,1,0] op_sel_hi:[0,1,0]
	ds_read_b128 v[24:27], v19 offset:41360
	ds_read_b128 v[28:31], v19 offset:41872
	ds_bpermute_b32 v14, v18, v14
	ds_bpermute_b32 v15, v18, v15
	ds_bpermute_b32 v16, v18, v16
	ds_bpermute_b32 v17, v18, v17
	v_max_f32_e32 v23, 0, v23
	v_max_f32_e32 v12, 0, v12
	v_cvt_pk_f16_f32 v12, v23, v12
	s_waitcnt lgkmcnt(4)
	v_fma_mix_f32 v19, v24, v4, v28 op_sel_hi:[0,1,0]
	v_fma_mix_f32 v4, v25, v4, v29 op_sel:[0,1,0] op_sel_hi:[0,1,0]
	v_fma_mix_f32 v23, v26, v5, v30 op_sel_hi:[0,1,0]
	v_fma_mix_f32 v5, v27, v5, v31 op_sel:[0,1,0] op_sel_hi:[0,1,0]
	v_max_f32_e32 v20, 0, v20
	v_max_f32_e32 v2, 0, v2
	v_max_f32_e32 v21, 0, v21
	v_max_f32_e32 v3, 0, v3
	v_max_f32_e32 v19, 0, v19
	v_max_f32_e32 v4, 0, v4
	v_max_f32_e32 v23, 0, v23
	v_max_f32_e32 v5, 0, v5
	v_cvt_pk_f16_f32 v5, v23, v5
	v_cvt_pk_f16_f32 v4, v19, v4
	v_cvt_pk_f16_f32 v3, v21, v3
	v_cvt_pk_f16_f32 v2, v20, v2
	ds_bpermute_b32 v6, v18, v6
	ds_bpermute_b32 v7, v18, v7
	ds_bpermute_b32 v8, v18, v8
	ds_bpermute_b32 v9, v18, v9
	ds_bpermute_b32 v10, v18, v10
	ds_bpermute_b32 v11, v18, v11
	ds_bpermute_b32 v12, v18, v12
	ds_bpermute_b32 v13, v18, v13
	ds_bpermute_b32 v2, v18, v2
	ds_bpermute_b32 v3, v18, v3
	ds_bpermute_b32 v4, v18, v4
	ds_bpermute_b32 v5, v18, v5
	ds_read_b128 v[18:21], v65
	ds_read_b128 v[22:25], v65 offset:4096
	ds_read_b128 v[26:29], v65 offset:8192
	ds_read_b128 v[42:45], v65 offset:12288
	s_waitcnt lgkmcnt(3)
	v_mfma_f32_16x16x32_f16 v[30:33], v[14:17], v[18:21], 0
	s_waitcnt lgkmcnt(2)
	v_mfma_f32_16x16x32_f16 v[34:37], v[14:17], v[22:25], 0
	ds_read_b128 v[18:21], v65 offset:16384
	ds_read_b128 v[22:25], v65 offset:20480
	ds_read_b128 v[46:49], v65 offset:24576
	ds_read_b128 v[50:53], v65 offset:28672
	s_waitcnt lgkmcnt(5)
	v_mfma_f32_16x16x32_f16 v[38:41], v[14:17], v[26:29], 0
	s_waitcnt lgkmcnt(4)
	v_mfma_f32_16x16x32_f16 v[42:45], v[14:17], v[42:45], 0
	s_waitcnt lgkmcnt(3)
	v_mfma_f32_16x16x32_f16 v[26:29], v[14:17], v[18:21], 0
	s_waitcnt lgkmcnt(2)
	v_mfma_f32_16x16x32_f16 v[22:25], v[14:17], v[22:25], 0
	s_waitcnt lgkmcnt(1)
	v_mfma_f32_16x16x32_f16 v[18:21], v[14:17], v[46:49], 0
	s_waitcnt lgkmcnt(0)
	v_mfma_f32_16x16x32_f16 v[14:17], v[14:17], v[50:53], 0
	ds_read_b128 v[46:49], v65 offset:1024
	ds_read_b128 v[50:53], v65 offset:5120
	ds_read_b128 v[54:57], v65 offset:9216
	ds_read_b128 v[58:61], v65 offset:13312
	s_waitcnt lgkmcnt(3)
	v_mfma_f32_16x16x32_f16 v[30:33], v[6:9], v[46:49], v[30:33]
	s_waitcnt lgkmcnt(2)
	v_mfma_f32_16x16x32_f16 v[34:37], v[6:9], v[50:53], v[34:37]
	s_waitcnt lgkmcnt(1)
	v_mfma_f32_16x16x32_f16 v[38:41], v[6:9], v[54:57], v[38:41]
	s_waitcnt lgkmcnt(0)
	v_mfma_f32_16x16x32_f16 v[42:45], v[6:9], v[58:61], v[42:45]
	ds_read_b128 v[58:61], v65 offset:17408
	ds_read_b128 v[54:57], v65 offset:21504
	ds_read_b128 v[50:53], v65 offset:25600
	ds_read_b128 v[46:49], v65 offset:29696
	s_waitcnt lgkmcnt(3)
	v_mfma_f32_16x16x32_f16 v[26:29], v[6:9], v[58:61], v[26:29]
	s_waitcnt lgkmcnt(2)
	v_mfma_f32_16x16x32_f16 v[22:25], v[6:9], v[54:57], v[22:25]
	s_waitcnt lgkmcnt(1)
	v_mfma_f32_16x16x32_f16 v[18:21], v[6:9], v[50:53], v[18:21]
	s_waitcnt lgkmcnt(0)
	v_mfma_f32_16x16x32_f16 v[14:17], v[6:9], v[46:49], v[14:17]
	ds_read_b128 v[6:9], v65 offset:2048
	ds_read_b128 v[46:49], v65 offset:6144
	ds_read_b128 v[50:53], v65 offset:10240
	ds_read_b128 v[54:57], v65 offset:14336
	s_waitcnt lgkmcnt(3)
	v_mfma_f32_16x16x32_f16 v[30:33], v[10:13], v[6:9], v[30:33]
	s_waitcnt lgkmcnt(2)
	v_mfma_f32_16x16x32_f16 v[46:49], v[10:13], v[46:49], v[34:37]
	s_waitcnt lgkmcnt(1)
	v_mfma_f32_16x16x32_f16 v[50:53], v[10:13], v[50:53], v[38:41]
	s_waitcnt lgkmcnt(0)
	v_mfma_f32_16x16x32_f16 v[42:45], v[10:13], v[54:57], v[42:45]
	ds_read_b128 v[6:9], v65 offset:18432
	ds_read_b128 v[34:37], v65 offset:22528
	ds_read_b128 v[38:41], v65 offset:26624
	ds_read_b128 v[54:57], v65 offset:30720
	s_waitcnt lgkmcnt(3)
	v_mfma_f32_16x16x32_f16 v[6:9], v[10:13], v[6:9], v[26:29]
	s_waitcnt lgkmcnt(2)
	v_mfma_f32_16x16x32_f16 v[26:29], v[10:13], v[34:37], v[22:25]
	s_waitcnt lgkmcnt(1)
	v_mfma_f32_16x16x32_f16 v[34:37], v[10:13], v[38:41], v[18:21]
	s_waitcnt lgkmcnt(0)
	v_mfma_f32_16x16x32_f16 v[38:41], v[10:13], v[54:57], v[14:17]
	ds_read_b128 v[10:13], v65 offset:3072
	s_nop 1
	ds_read_b128 v[14:17], v65 offset:7168
	ds_read_b128 v[54:57], v65 offset:11264
	ds_read_b128 v[58:61], v65 offset:15360
	s_waitcnt lgkmcnt(3)
	v_mfma_f32_16x16x32_f16 v[22:25], v[2:5], v[10:13], v[30:33]
	s_waitcnt lgkmcnt(2)
	v_mfma_f32_16x16x32_f16 v[18:21], v[2:5], v[14:17], v[46:49]
	s_waitcnt lgkmcnt(1)
	v_mfma_f32_16x16x32_f16 v[14:17], v[2:5], v[54:57], v[50:53]
	s_waitcnt lgkmcnt(0)
	v_mfma_f32_16x16x32_f16 v[10:13], v[2:5], v[58:61], v[42:45]
	ds_read_b128 v[30:33], v65 offset:19456
	s_nop 1
	ds_read_b128 v[42:45], v65 offset:23552
	ds_read_b128 v[46:49], v65 offset:27648
	ds_read_b128 v[50:53], v65 offset:31744
	v_lshlrev_b32_e32 v59, 2, v64
	v_lshlrev_b32_e32 v58, 10, v62
	s_waitcnt lgkmcnt(3)
	v_mfma_f32_16x16x32_f16 v[30:33], v[2:5], v[30:33], v[6:9]
	s_waitcnt lgkmcnt(1)
	v_mfma_f32_16x16x32_f16 v[6:9], v[2:5], v[46:49], v[34:37]
	s_nop 2
	v_lshlrev_b32_e32 v34, 3, v0
	v_mfma_f32_16x16x32_f16 v[26:29], v[2:5], v[42:45], v[26:29]
	v_and_b32_e32 v44, 0x78, v34
	v_lshlrev_b32_e32 v34, 4, v63
	v_ashrrev_i32_e32 v35, 31, v34
	v_lshl_add_u64 v[36:37], v[34:35], 2, s[8:9]
	v_and_b32_e32 v42, 48, v0
	v_mov_b32_e32 v43, 0
	v_lshl_add_u64 v[36:37], v[36:37], 0, v[42:43]
	v_lshlrev_b32_e32 v42, 1, v44
	v_lshlrev_b32_e32 v60, 2, v44
	s_waitcnt lgkmcnt(0)
	v_mfma_f32_16x16x32_f16 v[2:5], v[2:5], v[50:53], v[38:41]
	v_or_b32_e32 v48, v34, v59
	v_lshl_add_u64 v[46:47], s[12:13], 0, v[42:43]
	v_mov_b32_e32 v52, v14
	global_load_dwordx4 v[38:41], v[36:37], off
	s_nop 0
	global_load_dwordx4 v[34:37], v60, s[6:7] offset:16
	global_load_dwordx4 v[42:45], v60, s[6:7]
	v_mov_b32_e32 v53, v10
	v_mov_b32_e32 v50, v22
	v_mov_b32_e32 v51, v18
	v_ashrrev_i32_e32 v49, 31, v48
	v_mov_b32_e32 v18, v23
	v_mov_b32_e32 v10, v15
	v_lshlrev_b64 v[66:67], 8, v[48:49]
	v_lshl_add_u64 v[66:67], v[46:47], 0, v[66:67]
	s_waitcnt vmcnt(0)
	v_pk_add_f32 v[52:53], v[44:45], v[52:53]
	s_nop 0
	v_pk_mul_f32 v[54:55], v[38:39], v[52:53] op_sel_hi:[0,1]
	v_mov_b32_e32 v52, v30
	v_mov_b32_e32 v53, v26
	v_pk_add_f32 v[52:53], v[34:35], v[52:53]
	v_pk_add_f32 v[50:51], v[42:43], v[50:51]
	v_pk_mul_f32 v[56:57], v[38:39], v[52:53] op_sel_hi:[0,1]
	v_mov_b32_e32 v52, v6
	v_mov_b32_e32 v53, v2
	v_pk_add_f32 v[52:53], v[36:37], v[52:53]
	v_mov_b32_e32 v26, v31
	v_mov_b32_e32 v2, v7
	v_or_b32_e32 v6, 1, v48
	v_pk_mul_f32 v[50:51], v[38:39], v[50:51] op_sel_hi:[0,1]
	v_pk_mul_f32 v[52:53], v[38:39], v[52:53] op_sel_hi:[0,1]
	v_pk_add_f32 v[18:19], v[42:43], v[18:19]
	v_pk_add_f32 v[10:11], v[44:45], v[10:11]
	v_pk_add_f32 v[14:15], v[34:35], v[26:27]
	v_pk_add_f32 v[2:3], v[36:37], v[2:3]
	v_ashrrev_i32_e32 v7, 31, v6
	v_cvt_pk_f16_f32 v62, v50, v51
	v_cvt_pk_f16_f32 v63, v54, v55
	v_cvt_pk_f16_f32 v64, v56, v57
	v_cvt_pk_f16_f32 v65, v52, v53
	v_pk_mul_f32 v[18:19], v[38:39], v[18:19] op_sel:[1,0]
	v_pk_mul_f32 v[10:11], v[38:39], v[10:11] op_sel:[1,0]
	v_pk_mul_f32 v[22:23], v[38:39], v[14:15] op_sel:[1,0]
	v_pk_mul_f32 v[2:3], v[38:39], v[2:3] op_sel:[1,0]
	v_lshlrev_b64 v[6:7], 8, v[6:7]
	global_store_dwordx4 v[66:67], v[62:65], off sc0 sc1
	v_lshl_add_u64 v[6:7], v[46:47], 0, v[6:7]
	s_nop 0
	v_cvt_pk_f16_f32 v62, v18, v19
	v_cvt_pk_f16_f32 v63, v10, v11
	v_cvt_pk_f16_f32 v64, v22, v23
	v_cvt_pk_f16_f32 v65, v2, v3
	global_store_dwordx4 v[6:7], v[62:65], off sc0 sc1
	v_mov_b32_e32 v6, v24
	v_mov_b32_e32 v7, v20
	v_pk_add_f32 v[6:7], v[42:43], v[6:7]
	v_mov_b32_e32 v20, v25
	v_pk_mul_f32 v[14:15], v[40:41], v[6:7] op_sel_hi:[0,1]
	v_mov_b32_e32 v6, v16
	v_mov_b32_e32 v7, v12
	v_pk_add_f32 v[6:7], v[44:45], v[6:7]
	v_mov_b32_e32 v12, v17
	v_pk_mul_f32 v[30:31], v[40:41], v[6:7] op_sel_hi:[0,1]
	v_mov_b32_e32 v6, v32
	v_mov_b32_e32 v7, v28
	v_pk_add_f32 v[6:7], v[34:35], v[6:7]
	v_mov_b32_e32 v16, v41
	v_pk_mul_f32 v[38:39], v[40:41], v[6:7] op_sel_hi:[0,1]
	v_mov_b32_e32 v6, v8
	v_mov_b32_e32 v7, v4
	v_pk_add_f32 v[6:7], v[36:37], v[6:7]
	v_pk_add_f32 v[12:13], v[44:45], v[12:13]
	v_pk_mul_f32 v[26:27], v[40:41], v[6:7] op_sel_hi:[0,1]
	v_or_b32_e32 v6, 2, v48
	v_ashrrev_i32_e32 v7, 31, v6
	v_lshlrev_b64 v[6:7], 8, v[6:7]
	v_mov_b32_e32 v28, v33
	v_cvt_pk_f16_f32 v62, v14, v15
	v_cvt_pk_f16_f32 v63, v30, v31
	v_cvt_pk_f16_f32 v64, v38, v39
	v_cvt_pk_f16_f32 v65, v26, v27
	v_lshl_add_u64 v[6:7], v[46:47], 0, v[6:7]
	v_pk_mul_f32 v[24:25], v[16:17], v[12:13] op_sel_hi:[0,1]
	v_pk_add_f32 v[12:13], v[34:35], v[28:29]
	v_add_f32_e32 v4, 0, v52
	global_store_dwordx4 v[6:7], v[62:65], off sc0 sc1
	v_pk_add_f32 v[6:7], v[42:43], v[20:21]
	v_pk_mul_f32 v[28:29], v[16:17], v[12:13] op_sel_hi:[0,1]
	v_pk_mul_f32 v[12:13], v[2:3], v[2:3]
	v_add_f32_e32 v2, v2, v4
	v_pk_mul_f32 v[20:21], v[16:17], v[6:7] op_sel_hi:[0,1]
	v_add_f32_e32 v17, v26, v2
	v_add_f32_e32 v2, 0, v57
	v_add_f32_e32 v2, v23, v2
	v_pk_fma_f32 v[12:13], v[52:53], v[52:53], v[12:13]
	v_add_f32_e32 v2, v39, v2
	v_pk_fma_f32 v[32:33], v[26:27], v[26:27], v[12:13]
	v_pk_mul_f32 v[12:13], v[22:23], v[22:23]
	v_add_f32_e32 v26, v29, v2
	v_add_f32_e32 v2, 0, v56
	v_pk_fma_f32 v[12:13], v[56:57], v[56:57], v[12:13]
	v_add_f32_e32 v2, v22, v2
	v_pk_fma_f32 v[12:13], v[38:39], v[38:39], v[12:13]
	v_add_f32_e32 v2, v38, v2
	v_cvt_pk_f16_f32 v8, v28, v29
	v_pk_fma_f32 v[12:13], v[28:29], v[28:29], v[12:13]
	v_add_f32_e32 v28, v28, v2
	v_pk_mul_f32 v[22:23], v[10:11], v[10:11]
	v_add_f32_e32 v2, 0, v55
	v_pk_fma_f32 v[22:23], v[54:55], v[54:55], v[22:23]
	v_add_f32_e32 v2, v11, v2
	v_pk_fma_f32 v[22:23], v[30:31], v[30:31], v[22:23]
	v_add_f32_e32 v2, v31, v2
	v_cvt_pk_f16_f32 v7, v24, v25
	v_pk_fma_f32 v[22:23], v[24:25], v[24:25], v[22:23]
	v_add_f32_e32 v25, v25, v2
	v_add_f32_e32 v2, 0, v54
	v_add_f32_e32 v2, v10, v2
	v_add_f32_e32 v2, v30, v2
	v_add_f32_e32 v24, v24, v2
	v_add_f32_e32 v2, 0, v51
	v_pk_mul_f32 v[10:11], v[18:19], v[18:19]
	v_add_f32_e32 v2, v19, v2
	v_pk_fma_f32 v[10:11], v[50:51], v[50:51], v[10:11]
	v_add_f32_e32 v2, v15, v2
	v_pk_fma_f32 v[10:11], v[14:15], v[14:15], v[10:11]
	v_add_f32_e32 v15, v21, v2
	v_add_f32_e32 v2, 0, v50
	v_add_f32_e32 v2, v18, v2
	v_add_f32_e32 v2, v14, v2
	v_add_f32_e32 v14, v20, v2
	v_add_f32_e32 v2, 0, v53
	v_add_f32_e32 v2, v3, v2
	v_mov_b32_e32 v4, v9
	v_add_f32_e32 v18, v27, v2
	v_pk_add_f32 v[2:3], v[36:37], v[4:5]
	v_cvt_pk_f16_f32 v6, v20, v21
	v_pk_mul_f32 v[2:3], v[16:17], v[2:3] op_sel_hi:[0,1]
	v_cvt_pk_f16_f32 v9, v2, v3
	v_pk_fma_f32 v[4:5], v[2:3], v[2:3], v[32:33]
	v_add_f32_e32 v16, v2, v17
	v_or_b32_e32 v2, 3, v48
	v_add_f32_e32 v17, v3, v18
	v_ashrrev_i32_e32 v3, 31, v2
	v_lshlrev_b64 v[2:3], 8, v[2:3]
	v_lshl_add_u64 v[2:3], v[46:47], 0, v[2:3]
	v_permlane16_swap_b32_e32 v14, v15
	v_permlane16_swap_b32_e32 v24, v25
	global_store_dwordx4 v[2:3], v[6:9], off sc0 sc1
	v_add_f32_e32 v2, v14, v15
	v_add_f32_e32 v3, v24, v25
	v_permlane16_swap_b32_e32 v28, v26
	v_permlane16_swap_b32_e32 v16, v17
	v_permlane32_swap_b32_e32 v2, v3
	v_add_f32_e32 v6, v28, v26
	v_add_f32_e32 v7, v16, v17
	v_add_f32_e32 v2, v2, v3
	v_or3_b32 v3, v58, v60, v59
	v_permlane32_swap_b32_e32 v6, v7
	v_pk_fma_f32 v[10:11], v[20:21], v[20:21], v[10:11]
	v_add_f32_e32 v6, v6, v7
	v_add_u32_e32 v3, 0x8000, v3
	ds_write2_b32 v3, v2, v6 offset1:4
	v_mov_b32_e32 v2, v11
	v_mov_b32_e32 v6, v23
	s_nop 0
	v_permlane16_swap_b32_e32 v10, v2
	v_permlane16_swap_b32_e32 v22, v6
	v_add_f32_e32 v2, v10, v2
	v_add_f32_e32 v6, v22, v6
	s_nop 1
	v_permlane32_swap_b32_e32 v2, v6
	v_add_f32_e32 v2, v2, v6
	v_mov_b32_e32 v6, v13
	s_nop 1
	v_permlane16_swap_b32_e32 v12, v6
	v_permlane16_swap_b32_e32 v4, v5
	v_add_f32_e32 v6, v12, v6
	v_add_f32_e32 v4, v4, v5
	s_nop 1
	v_permlane32_swap_b32_e32 v6, v4
	v_add_f32_e32 v4, v6, v4
	ds_write2_b32 v3, v2, v4 offset0:128 offset1:132

amdhsa.kernels:
  - .agpr_count:     0
    .args:
      - .actual_access:  read_only
        .address_space:  global
        .offset:         0
        .size:           8
        .value_kind:     global_buffer
      - .actual_access:  read_only
        .address_space:  global
        .offset:         8
        .size:           8
        .value_kind:     global_buffer
      - .actual_access:  write_only
        .address_space:  global
        .offset:         16
        .size:           8
        .value_kind:     global_buffer
      - .actual_access:  write_only
        .address_space:  global
        .offset:         24
        .size:           8
        .value_kind:     global_buffer
      - .actual_access:  read_only
        .address_space:  global
        .offset:         32
        .size:           8
        .value_kind:     global_buffer
      - .actual_access:  read_only
        .address_space:  global
        .offset:         40
        .size:           8
        .value_kind:     global_buffer
      - .actual_access:  read_only
        .address_space:  global
        .offset:         48
        .size:           8
        .value_kind:     global_buffer
      - .actual_access:  read_only
        .address_space:  global
        .offset:         56
        .size:           8
        .value_kind:     global_buffer
      - .actual_access:  read_only
        .address_space:  global
        .offset:         64
        .size:           8
        .value_kind:     global_buffer
      - .actual_access:  read_only
        .address_space:  global
        .offset:         72
        .size:           8
        .value_kind:     global_buffer
      - .actual_access:  read_only
        .address_space:  global
        .offset:         80
        .size:           8
        .value_kind:     global_buffer
      - .actual_access:  write_only
        .address_space:  global
        .offset:         88
        .size:           8
        .value_kind:     global_buffer
      - .actual_access:  write_only
        .address_space:  global
        .offset:         96
        .size:           8
        .value_kind:     global_buffer
      - .actual_access:  write_only
        .address_space:  global
        .offset:         104
        .size:           8
        .value_kind:     global_buffer
      - .offset:         112
        .size:           4
        .value_kind:     by_value
      - .actual_access:  write_only
        .address_space:  global
        .offset:         120
        .size:           8
        .value_kind:     global_buffer
      - .offset:         128
        .size:           4
        .value_kind:     by_value
    .group_segment_fixed_size: 38944
    .kernarg_segment_align: 8
    .kernarg_segment_size: 132
    .language:       OpenCL C
    .language_version:
      - 2
      - 0
    .max_flat_workgroup_size: 512
    .name:           _Z6k_pre1PK15HIP_vector_typeIiLj4EES2_PiPjPKfS6_S6_S6_S6_S6_S6_PDF16_S7_S3_iS3_i
    .private_segment_fixed_size: 0
    .sgpr_count:     28
    .sgpr_spill_count: 0
    .symbol:         _Z6k_pre1PK15HIP_vector_typeIiLj4EES2_PiPjPKfS6_S6_S6_S6_S6_S6_PDF16_S7_S3_iS3_i.kd
    .uniform_work_group_size: 1
    .uses_dynamic_stack: false
    .vgpr_count:     61
    .vgpr_spill_count: 0
    .wavefront_size: 64
  - .agpr_count:     0
    .args:
      - .actual_access:  read_only
        .address_space:  global
        .offset:         0
        .size:           8
        .value_kind:     global_buffer
      - .actual_access:  read_only
        .address_space:  global
        .offset:         8
        .size:           8
        .value_kind:     global_buffer
      - .actual_access:  write_only
        .address_space:  global
        .offset:         16
        .size:           8
        .value_kind:     global_buffer
      - .actual_access:  write_only
        .address_space:  global
        .offset:         24
        .size:           8
        .value_kind:     global_buffer
      - .actual_access:  read_only
        .address_space:  global
        .offset:         32
        .size:           8
        .value_kind:     global_buffer
      - .actual_access:  read_only
        .address_space:  global
        .offset:         40
        .size:           8
        .value_kind:     global_buffer
      - .actual_access:  read_only
        .address_space:  global
        .offset:         48
        .size:           8
        .value_kind:     global_buffer
      - .actual_access:  read_only
        .address_space:  global
        .offset:         56
        .size:           8
        .value_kind:     global_buffer
      - .actual_access:  read_only
        .address_space:  global
        .offset:         64
        .size:           8
        .value_kind:     global_buffer
      - .actual_access:  write_only
        .address_space:  global
        .offset:         72
        .size:           8
        .value_kind:     global_buffer
      - .actual_access:  write_only
        .address_space:  global
        .offset:         80
        .size:           8
        .value_kind:     global_buffer
      - .actual_access:  write_only
        .address_space:  global
        .offset:         88
        .size:           8
        .value_kind:     global_buffer
      - .offset:         96
        .size:           4
        .value_kind:     hidden_block_count_x
      - .offset:         100
        .size:           4
        .value_kind:     hidden_block_count_y
      - .offset:         104
        .size:           4
        .value_kind:     hidden_block_count_z
      - .offset:         108
        .size:           2
        .value_kind:     hidden_group_size_x
      - .offset:         110
        .size:           2
        .value_kind:     hidden_group_size_y
      - .offset:         112
        .size:           2
        .value_kind:     hidden_group_size_z
      - .offset:         114
        .size:           2
        .value_kind:     hidden_remainder_x
      - .offset:         116
        .size:           2
        .value_kind:     hidden_remainder_y
      - .offset:         118
        .size:           2
        .value_kind:     hidden_remainder_z
      - .offset:         136
        .size:           8
        .value_kind:     hidden_global_offset_x
      - .offset:         144
        .size:           8
        .value_kind:     hidden_global_offset_y
      - .offset:         152
        .size:           8
        .value_kind:     hidden_global_offset_z
      - .offset:         160
        .size:           2
        .value_kind:     hidden_grid_dims
    .group_segment_fixed_size: 63520
    .kernarg_segment_align: 8
    .kernarg_segment_size: 352
    .language:       OpenCL C
    .language_version:
      - 2
      - 0
    .max_flat_workgroup_size: 512
    .name:           _Z6k_pre2PKjPKiPiS3_PKfPKDv8_DF16_S5_S8_S2_PDF16_PhPf
    .private_segment_fixed_size: 0
    .sgpr_count:     36
    .sgpr_spill_count: 0
    .symbol:         _Z6k_pre2PKjPKiPiS3_PKfPKDv8_DF16_S5_S8_S2_PDF16_PhPf.kd
    .uniform_work_group_size: 1
    .uses_dynamic_stack: false
    .vgpr_count:     107
    .vgpr_spill_count: 0
    .wavefront_size: 64
  - .agpr_count:     0
    .args:
      - .actual_access:  read_only
        .address_space:  global
        .offset:         0
        .size:           8
        .value_kind:     global_buffer
      - .actual_access:  read_only
        .address_space:  global
        .offset:         8
        .size:           8
        .value_kind:     global_buffer
      - .actual_access:  read_only
        .address_space:  global
        .offset:         16
        .size:           8
        .value_kind:     global_buffer
      - .actual_access:  read_only
        .address_space:  global
        .offset:         24
        .size:           8
        .value_kind:     global_buffer
      - .actual_access:  read_only
        .address_space:  global
        .offset:         32
        .size:           8
        .value_kind:     global_buffer
      - .actual_access:  read_only
        .address_space:  global
        .offset:         40
        .size:           8
        .value_kind:     global_buffer
      - .actual_access:  write_only
        .address_space:  global
        .offset:         48
        .size:           8
        .value_kind:     global_buffer
      - .address_space:  global
        .offset:         56
        .size:           8
        .value_kind:     global_buffer
      - .offset:         64
        .size:           4
        .value_kind:     hidden_block_count_x
      - .offset:         68
        .size:           4
        .value_kind:     hidden_block_count_y
      - .offset:         72
        .size:           4
        .value_kind:     hidden_block_count_z
      - .offset:         76
        .size:           2
        .value_kind:     hidden_group_size_x
      - .offset:         78
        .size:           2
        .value_kind:     hidden_group_size_y
      - .offset:         80
        .size:           2
        .value_kind:     hidden_group_size_z
      - .offset:         82
        .size:           2
        .value_kind:     hidden_remainder_x
      - .offset:         84
        .size:           2
        .value_kind:     hidden_remainder_y
      - .offset:         86
        .size:           2
        .value_kind:     hidden_remainder_z
      - .offset:         104
        .size:           8
        .value_kind:     hidden_global_offset_x
      - .offset:         112
        .size:           8
        .value_kind:     hidden_global_offset_y
      - .offset:         120
        .size:           8
        .value_kind:     hidden_global_offset_z
      - .offset:         128
        .size:           2
        .value_kind:     hidden_grid_dims
    .group_segment_fixed_size: 36864
    .kernarg_segment_align: 8
    .kernarg_segment_size: 320
    .language:       OpenCL C
    .language_version:
      - 2
      - 0
    .max_flat_workgroup_size: 256
    .name:           _Z5k_aggPKDF16_PKhPKiS4_PKDv8_DF16_PKfPDF16_Pf
    .private_segment_fixed_size: 0
    .sgpr_count:     25
    .sgpr_spill_count: 0
    .symbol:         _Z5k_aggPKDF16_PKhPKiS4_PKDv8_DF16_PKfPDF16_Pf.kd
    .uniform_work_group_size: 1
    .uses_dynamic_stack: false
    .vgpr_count:     108
    .vgpr_spill_count: 0
    .wavefront_size: 64
  - .agpr_count:     0
    .args:
      - .actual_access:  read_only
        .address_space:  global
        .offset:         0
        .size:           8
        .value_kind:     global_buffer
      - .actual_access:  read_only
        .address_space:  global
        .offset:         8
        .size:           8
        .value_kind:     global_buffer
      - .actual_access:  write_only
        .address_space:  global
        .offset:         16
        .size:           8
        .value_kind:     global_buffer
      - .offset:         24
        .size:           4
        .value_kind:     hidden_block_count_x
      - .offset:         28
        .size:           4
        .value_kind:     hidden_block_count_y
      - .offset:         32
        .size:           4
        .value_kind:     hidden_block_count_z
      - .offset:         36
        .size:           2
        .value_kind:     hidden_group_size_x
      - .offset:         38
        .size:           2
        .value_kind:     hidden_group_size_y
      - .offset:         40
        .size:           2
        .value_kind:     hidden_group_size_z
      - .offset:         42
        .size:           2
        .value_kind:     hidden_remainder_x
      - .offset:         44
        .size:           2
        .value_kind:     hidden_remainder_y
      - .offset:         46
        .size:           2
        .value_kind:     hidden_remainder_z
      - .offset:         64
        .size:           8
        .value_kind:     hidden_global_offset_x
      - .offset:         72
        .size:           8
        .value_kind:     hidden_global_offset_y
      - .offset:         80
        .size:           8
        .value_kind:     hidden_global_offset_z
      - .offset:         88
        .size:           2
        .value_kind:     hidden_grid_dims
    .group_segment_fixed_size: 0
    .kernarg_segment_align: 8
    .kernarg_segment_size: 280
    .language:       OpenCL C
    .language_version:
      - 2
      - 0
    .max_flat_workgroup_size: 1024
    .name:           _Z5k_outPKiPKfPf
    .private_segment_fixed_size: 0
    .sgpr_count:     14
    .sgpr_spill_count: 0
    .symbol:         _Z5k_outPKiPKfPf.kd
    .uniform_work_group_size: 1
    .uses_dynamic_stack: false
    .vgpr_count:     44
    .vgpr_spill_count: 0
    .wavefront_size: 64
  - .agpr_count:     0
    .args:
      - .address_space:  global
        .offset:         0
        .size:           8
        .value_kind:     global_buffer
      - .actual_access:  read_only
        .address_space:  global
        .offset:         8
        .size:           8
        .value_kind:     global_buffer
      - .actual_access:  read_only
        .address_space:  global
        .offset:         16
        .size:           8
        .value_kind:     global_buffer
      - .actual_access:  read_only
        .address_space:  global
        .offset:         24
        .size:           8
        .value_kind:     global_buffer
      - .actual_access:  read_only
        .address_space:  global
        .offset:         32
        .size:           8
        .value_kind:     global_buffer
      - .actual_access:  read_only
        .address_space:  global
        .offset:         40
        .size:           8
        .value_kind:     global_buffer
      - .actual_access:  read_only
        .address_space:  global
        .offset:         48
        .size:           8
        .value_kind:     global_buffer
      - .address_space:  global
        .offset:         56
        .size:           8
        .value_kind:     global_buffer
      - .offset:         64
        .size:           4
        .value_kind:     hidden_block_count_x
      - .offset:         68
        .size:           4
        .value_kind:     hidden_block_count_y
      - .offset:         72
        .size:           4
        .value_kind:     hidden_block_count_z
      - .offset:         76
        .size:           2
        .value_kind:     hidden_group_size_x
      - .offset:         78
        .size:           2
        .value_kind:     hidden_group_size_y
      - .offset:         80
        .size:           2
        .value_kind:     hidden_group_size_z
      - .offset:         82
        .size:           2
        .value_kind:     hidden_remainder_x
      - .offset:         84
        .size:           2
        .value_kind:     hidden_remainder_y
      - .offset:         86
        .size:           2
        .value_kind:     hidden_remainder_z
      - .offset:         104
        .size:           8
        .value_kind:     hidden_global_offset_x
      - .offset:         112
        .size:           8
        .value_kind:     hidden_global_offset_y
      - .offset:         120
        .size:           8
        .value_kind:     hidden_global_offset_z
      - .offset:         128
        .size:           2
        .value_kind:     hidden_grid_dims
    .group_segment_fixed_size: 41984
    .kernarg_segment_align: 8
    .kernarg_segment_size: 320
    .language:       OpenCL C
    .language_version:
      - 2
      - 0
    .max_flat_workgroup_size: 512
    .name:           _Z6k_mlp2ILi0EEvPDF16_PKfS2_S2_PKDv8_DF16_S2_S2_Pf
    .private_segment_fixed_size: 0
    .sgpr_count:     29
    .sgpr_spill_count: 0
    .symbol:         _Z6k_mlp2ILi0EEvPDF16_PKfS2_S2_PKDv8_DF16_S2_S2_Pf.kd
    .uniform_work_group_size: 1
    .uses_dynamic_stack: false
    .vgpr_count:     76
    .vgpr_spill_count: 0
    .wavefront_size: 64
  - .agpr_count:     0
    .args:
      - .actual_access:  read_only
        .address_space:  global
        .offset:         0
        .size:           8
        .value_kind:     global_buffer
      - .actual_access:  read_only
        .address_space:  global
        .offset:         8
        .size:           8
        .value_kind:     global_buffer
      - .actual_access:  read_only
        .address_space:  global
        .offset:         16
        .size:           8
        .value_kind:     global_buffer
      - .actual_access:  read_only
        .address_space:  global
        .offset:         24
        .size:           8
        .value_kind:     global_buffer
      - .address_space:  global
        .offset:         32
        .size:           8
        .value_kind:     global_buffer
      - .actual_access:  write_only
        .address_space:  global
        .offset:         40
        .size:           8
        .value_kind:     global_buffer
      - .actual_access:  read_only
        .address_space:  global
        .offset:         48
        .size:           8
        .value_kind:     global_buffer
      - .actual_access:  read_only
        .address_space:  global
        .offset:         56
        .size:           8
        .value_kind:     global_buffer
      - .actual_access:  read_only
        .address_space:  global
        .offset:         64
        .size:           8
        .value_kind:     global_buffer
      - .address_space:  global
        .offset:         72
        .size:           8
        .value_kind:     global_buffer
    .group_segment_fixed_size: 1024
    .kernarg_segment_align: 8
    .kernarg_segment_size: 80
    .language:       OpenCL C
    .language_version:
      - 2
      - 0
    .max_flat_workgroup_size: 512
    .name:           _Z8k_updateILi1EEvPKDF16_PKfS3_S3_PDF16_PhPKDv8_DF16_PKiPfSB_
    .private_segment_fixed_size: 0
    .sgpr_count:     25
    .sgpr_spill_count: 0
    .symbol:         _Z8k_updateILi1EEvPKDF16_PKfS3_S3_PDF16_PhPKDv8_DF16_PKiPfSB_.kd
    .uniform_work_group_size: 1
    .uses_dynamic_stack: false
    .vgpr_count:     112
    .vgpr_spill_count: 0
    .wavefront_size: 64
  - .agpr_count:     0
    .args:
      - .actual_access:  read_only
        .address_space:  global
        .offset:         0
        .size:           8
        .value_kind:     global_buffer
      - .actual_access:  read_only
        .address_space:  global
        .offset:         8
        .size:           8
        .value_kind:     global_buffer
      - .actual_access:  read_only
        .address_space:  global
        .offset:         16
        .size:           8
        .value_kind:     global_buffer
      - .actual_access:  read_only
        .address_space:  global
        .offset:         24
        .size:           8
        .value_kind:     global_buffer
      - .actual_access:  read_only
        .address_space:  global
        .offset:         32
        .size:           8
        .value_kind:     global_buffer
      - .actual_access:  read_only
        .address_space:  global
        .offset:         40
        .size:           8
        .value_kind:     global_buffer
      - .actual_access:  read_only
        .address_space:  global
        .offset:         48
        .size:           8
        .value_kind:     global_buffer
      - .actual_access:  read_only
        .address_space:  global
        .offset:         56
        .size:           8
        .value_kind:     global_buffer
      - .address_space:  global
        .offset:         64
        .size:           8
        .value_kind:     global_buffer
      - .actual_access:  read_only
        .address_space:  global
        .offset:         72
        .size:           8
        .value_kind:     global_buffer
    .group_segment_fixed_size: 6656
    .kernarg_segment_align: 8
    .kernarg_segment_size: 80
    .language:       OpenCL C
    .language_version:
      - 2
      - 0
    .max_flat_workgroup_size: 512
    .name:           _Z8k_updateILi2EEvPKDF16_PKfS3_S3_PDF16_PhPKDv8_DF16_PKiPfSB_
    .private_segment_fixed_size: 0
    .sgpr_count:     36
    .sgpr_spill_count: 0
    .symbol:         _Z8k_updateILi2EEvPKDF16_PKfS3_S3_PDF16_PhPKDv8_DF16_PKiPfSB_.kd
    .uniform_work_group_size: 1
    .uses_dynamic_stack: false
    .vgpr_count:     104
    .vgpr_spill_count: 0
    .wavefront_size: 64
